# speedup vs baseline: 1.0008x; 1.0008x over previous
_ZN4attn11attn_kernelEPKDF16_S1_S1_PDF16_PKyPKh:
	s_cmpk_lt_u32 s2, 0x100
	s_cbranch_scc0 .Lattn_done
	s_mov_b64 s[44:45], s[0:1]
	s_mov_b32 s46, s2
	s_mov_b32 s47, 0
	v_mov_b32_e32 v220, v0
.Lattn_again:
	s_load_dwordx4 s[12:15], s[0:1], 0x20
	s_load_dwordx8 s[4:11], s[0:1], 0x0
	s_lshl_b32 s0, s2, 3
	s_and_b32 s0, s0, 56
	s_lshr_b32 s1, s2, 6
	s_add_i32 s16, s0, s1
	s_lshl_b32 s1, s2, 5
	s_waitcnt lgkmcnt(0)
	v_mov_b32_e32 v2, s14
	s_lshr_b32 s14, s16, 4
	v_and_b32_e32 v201, 31, v0
	s_and_b32 s2, s1, 0x700
	v_lshrrev_b32_e32 v1, 1, v0
	v_mov_b32_e32 v3, s15
	s_lshl_b32 s0, s14, 11
	v_and_b32_e32 v1, 0xe0, v1
	v_or_b32_e32 v4, s2, v201
	s_mov_b32 s15, 0
	v_readfirstlane_b32 s20, v0
	v_or3_b32 v188, v4, v1, s0
	s_lshr_b32 s29, s20, 6
	s_lshl_b64 s[0:1], s[14:15], 11
	s_or_b32 s0, s0, s2
	s_lshl_b32 s2, s29, 5
	s_add_u32 s0, s0, s2
	s_addc_u32 s1, s1, 0
	s_lshl_b64 s[2:3], s[0:1], 11
	s_add_u32 s2, s4, s2
	s_addc_u32 s3, s5, s3
	s_lshl_b32 s21, s16, 6
	s_and_b32 s4, s21, 0x3c0
	v_mov_b32_e32 v189, 0
	s_lshl_b32 s28, s4, 1
	v_lshl_add_u64 v[2:3], v[188:189], 3, v[2:3]
	s_add_u32 s4, s2, s28
	global_load_dwordx2 v[2:3], v[2:3], off
	s_addc_u32 s5, s3, 0
	s_lshl_b64 s[2:3], s[14:15], 22
	s_add_u32 s14, s6, s2
	s_addc_u32 s17, s7, s3
	s_add_u32 s16, s14, s28
	s_addc_u32 s17, s17, 0
	s_add_u32 s14, s8, s2
	v_and_b32_e32 v182, 63, v0
	s_addc_u32 s19, s9, s3
	s_add_u32 s18, s14, s28
	v_lshlrev_b32_e32 v188, 11, v182
	s_addc_u32 s19, s19, 0
	v_lshl_add_u64 v[4:5], s[16:17], 0, v[188:189]
	s_lshl_b32 s14, s29, 4
	v_bfe_u32 v1, v0, 2, 4
	s_lshr_b32 s24, s20, 2
	v_lshl_add_u64 v[82:83], v[4:5], 0, s[14:15]
	v_and_or_b32 v4, s24, 48, v1
	v_lshlrev_b32_e32 v4, 11, v4
	v_mov_b32_e32 v5, v189
	v_lshlrev_b32_e32 v183, 3, v0
	v_lshl_add_u64 v[4:5], s[18:19], 0, v[4:5]
	s_and_b32 s14, s24, 0x3fffffc0
	v_and_b32_e32 v202, 24, v183
	v_lshl_add_u64 v[4:5], v[4:5], 0, s[14:15]
	v_lshlrev_b32_e32 v6, 1, v202
	v_mov_b32_e32 v7, v189
	s_lshl_b32 s34, s29, 10
	s_mov_b32 s16, m0
	s_mov_b32 m0, s34
	s_nop 0
	global_load_lds_dwordx4 v[82:83], off
	s_mov_b32 m0, s16
	s_mov_b64 s[18:19], 0x20000
	v_lshl_add_u64 v[190:191], v[4:5], 0, v[6:7]
	s_add_i32 s35, s34, 0x6000
	s_mov_b32 s16, m0
	s_mov_b32 m0, s35
	s_nop 0
	global_load_lds_dwordx4 v[190:191], off
	s_mov_b32 m0, s16
	v_lshl_add_u64 v[4:5], v[82:83], 0, s[18:19]
	v_bfe_u32 v200, v0, 5, 1
	s_add_i32 s16, s34, 0x2000
	s_mov_b32 s17, m0
	s_mov_b32 m0, s16
	s_nop 0
	global_load_lds_dwordx4 v[4:5], off
	s_mov_b32 m0, s17
	v_lshlrev_b32_e32 v4, 11, v201
	v_mov_b32_e32 v5, v189
	v_lshl_add_u64 v[4:5], s[4:5], 0, v[4:5]
	v_lshlrev_b32_e32 v184, 4, v200
	v_mov_b32_e32 v185, v189
	v_lshl_add_u64 v[4:5], v[4:5], 0, v[184:185]
	global_load_dwordx4 v[138:141], v[4:5], off
	global_load_dwordx4 v[130:133], v[4:5], off offset:32
	global_load_dwordx4 v[126:129], v[4:5], off offset:64
	global_load_dwordx4 v[118:121], v[4:5], off offset:96
	v_mov_b32_e32 v16, v189
	v_mov_b32_e32 v17, v189
	v_mov_b32_e32 v4, v189
	v_mov_b32_e32 v5, v189
	v_mov_b32_e32 v9, v189
	v_mov_b32_e32 v10, v189
	v_mov_b32_e32 v11, v189
	v_mov_b32_e32 v12, v189
	v_mov_b32_e32 v13, v189
	v_mov_b32_e32 v14, v189
	v_mov_b32_e32 v15, v189
	s_mov_b64 s[16:17], 0x40000
	v_lshl_add_u64 v[34:35], v[82:83], 0, s[16:17]
	s_add_i32 s5, s34, 0x4000
	s_movk_i32 s4, 0xf0
	s_mov_b32 s26, -1
	s_movk_i32 s27, 0x2000
	s_movk_i32 s23, 0x4000
	s_waitcnt vmcnt(4)
	v_and_b32_e32 v6, 15, v2
	v_lshrrev_b32_e32 v7, 4, v2
	v_lshrrev_b32_e32 v8, 8, v2
	v_lshrrev_b32_e32 v2, 12, v2
	v_and_b32_e32 v37, 0xf000, v2
	v_lshrrev_b32_e32 v2, 8, v3
	v_and_b32_e32 v7, 0xf0, v7
	v_and_b32_e32 v8, 0xf00, v8
	v_and_b32_e32 v40, 0xf00, v2
	v_lshlrev_b32_e32 v2, 4, v201
	v_or3_b32 v36, v7, v6, v8
	v_and_b32_e32 v38, 15, v3
	v_lshrrev_b32_e32 v39, 4, v3
	v_lshrrev_b32_e32 v41, 12, v3
	v_lshl_or_b32 v206, v200, 10, v2
	v_mov_b32_e32 v2, v189
	v_mov_b32_e32 v3, v189
	v_mov_b32_e32 v6, v189
	v_mov_b32_e32 v7, v189
	v_mov_b32_e32 v8, v189
	v_mov_b64_e32 v[32:33], v[16:17]
	v_mov_b64_e32 v[30:31], v[14:15]
	v_mov_b64_e32 v[28:29], v[12:13]
	v_mov_b64_e32 v[26:27], v[10:11]
	v_mov_b64_e32 v[24:25], v[8:9]
	v_mov_b64_e32 v[22:23], v[6:7]
	v_mov_b64_e32 v[20:21], v[4:5]
	v_mov_b64_e32 v[18:19], v[2:3]
	s_mov_b32 s22, m0
	s_mov_b32 m0, s5
	s_nop 0
	global_load_lds_dwordx4 v[34:35], off
	s_mov_b32 m0, s22
	s_waitcnt vmcnt(3) lgkmcnt(0)
	s_barrier
	ds_read_b128 v[50:53], v206
	ds_read_b128 v[54:57], v206 offset:512
	v_and_b32_e32 v34, 0xf000, v41
	v_and_or_b32 v35, v39, s4, v38
	v_or3_b32 v34, v35, v40, v34
	v_lshlrev_b32_e32 v34, 16, v34
	v_or3_b32 v58, v36, v37, v34
	v_mbcnt_lo_u32_b32 v34, -1, 0
	v_mbcnt_hi_u32_b32 v59, -1, v34
	s_waitcnt vmcnt(3) lgkmcnt(1)
	v_mfma_f32_32x32x16_f16 v[34:49], v[50:53], v[138:141], v[18:33]
	v_and_b32_e32 v50, 64, v59
	v_add_u32_e32 v60, 64, v50
	v_xor_b32_e32 v50, 1, v59
	v_cmp_lt_i32_e32 vcc, v50, v60
	s_mov_b32 s22, 16
	s_nop 0
	v_cndmask_b32_e32 v50, v59, v50, vcc
	v_lshlrev_b32_e32 v50, 2, v50
	ds_bpermute_b32 v61, v50, v58
	ds_read_b128 v[50:53], v206 offset:2048
	s_waitcnt lgkmcnt(2)
	v_mfma_f32_32x32x16_f16 v[18:33], v[54:57], v[138:141], v[18:33]
	v_xor_b32_e32 v54, 2, v59
	v_cmp_lt_i32_e32 vcc, v54, v60
	s_waitcnt lgkmcnt(1)
	v_or_b32_e32 v58, v61, v58
	v_cndmask_b32_e32 v54, v59, v54, vcc
	v_lshlrev_b32_e32 v61, 2, v54
	ds_read_b128 v[54:57], v206 offset:2560
	s_waitcnt vmcnt(2) lgkmcnt(1)
	v_mfma_f32_32x32x16_f16 v[34:49], v[50:53], v[130:133], v[34:49]
	ds_bpermute_b32 v50, v61, v58
	s_waitcnt lgkmcnt(0)
	v_or_b32_e32 v58, v50, v58
	v_xor_b32_e32 v50, 4, v59
	v_cmp_lt_i32_e32 vcc, v50, v60
	v_mfma_f32_32x32x16_f16 v[18:33], v[54:57], v[130:133], v[18:33]
	v_xor_b32_e32 v54, 8, v59
	v_cndmask_b32_e32 v50, v59, v50, vcc
	v_lshlrev_b32_e32 v50, 2, v50
	ds_bpermute_b32 v61, v50, v58
	ds_read_b128 v[50:53], v206 offset:4096
	v_cmp_lt_i32_e32 vcc, v54, v60
	s_waitcnt lgkmcnt(1)
	v_or_b32_e32 v58, v61, v58
	v_cndmask_b32_e32 v54, v59, v54, vcc
	v_lshlrev_b32_e32 v61, 2, v54
	ds_read_b128 v[54:57], v206 offset:4608
	s_waitcnt vmcnt(1) lgkmcnt(1)
	v_mfma_f32_32x32x16_f16 v[34:49], v[50:53], v[126:129], v[34:49]
	ds_bpermute_b32 v50, v61, v58
	s_waitcnt lgkmcnt(0)
	v_or_b32_e32 v58, v50, v58
	v_xor_b32_e32 v50, 16, v59
	v_cmp_lt_i32_e32 vcc, v50, v60
	v_mfma_f32_32x32x16_f16 v[18:33], v[54:57], v[126:129], v[18:33]
	s_nop 0
	v_cndmask_b32_e32 v50, v59, v50, vcc
	v_lshlrev_b32_e32 v59, 2, v50
	ds_bpermute_b32 v54, v59, v58
	ds_read_b128 v[50:53], v206 offset:6144
	s_waitcnt lgkmcnt(1)
	v_or_b32_e32 v54, v54, v58
	s_nop 0
	v_readfirstlane_b32 s33, v54
	ds_read_b128 v[54:57], v206 offset:6656
	s_waitcnt vmcnt(0) lgkmcnt(1)
	v_mfma_f32_32x32x16_f16 v[34:49], v[50:53], v[118:121], v[34:49]
	v_or_b32_e32 v50, s0, v201
	v_mov_b32_e32 v51, s1
	v_lshlrev_b64 v[50:51], 8, v[50:51]
	v_lshl_add_u64 v[186:187], s[12:13], 0, v[50:51]
	s_bitcmp0_b32 s33, 0
	s_waitcnt lgkmcnt(0)
	v_mfma_f32_32x32x16_f16 v[18:33], v[54:57], v[118:121], v[18:33]
	s_cbranch_scc0 .LBB1_59

.LBB1_58:
	s_lshl_b64 s[0:1], s[4:5], 1
	s_add_u32 s0, s10, s0
	s_addc_u32 s1, s11, s1
	s_lshl_b32 s2, s29, 12
	v_lshlrev_b32_e32 v0, 9, v200
	v_or3_b32 v0, s2, v0, v50
	v_fma_mixlo_f16 v1, v18, v69, 0
	ds_write_b16 v0, v1 offset:51200
	v_fma_mixlo_f16 v1, v2, v69, 0
	ds_write_b16 v0, v1 offset:51264
	v_fma_mixlo_f16 v1, v19, v68, 0
	ds_write_b16 v0, v1 offset:51328
	v_fma_mixlo_f16 v1, v3, v68, 0
	ds_write_b16 v0, v1 offset:51392
	v_fma_mixlo_f16 v1, v20, v67, 0
	ds_write_b16 v0, v1 offset:51456
	v_fma_mixlo_f16 v1, v4, v67, 0
	ds_write_b16 v0, v1 offset:51520
	v_fma_mixlo_f16 v1, v21, v66, 0
	ds_write_b16 v0, v1 offset:51584
	v_fma_mixlo_f16 v1, v5, v66, 0
	ds_write_b16 v0, v1 offset:51648
	v_fma_mixlo_f16 v1, v22, v64, 0
	ds_write_b16 v0, v1 offset:52224
	v_fma_mixlo_f16 v1, v6, v64, 0
	ds_write_b16 v0, v1 offset:52288
	v_fma_mixlo_f16 v1, v23, v65, 0
	ds_write_b16 v0, v1 offset:52352
	v_fma_mixlo_f16 v1, v7, v65, 0
	ds_write_b16 v0, v1 offset:52416
	v_fma_mixlo_f16 v1, v24, v63, 0
	ds_write_b16 v0, v1 offset:52480
	v_fma_mixlo_f16 v1, v8, v63, 0
	ds_write_b16 v0, v1 offset:52544
	v_fma_mixlo_f16 v1, v25, v61, 0
	ds_write_b16 v0, v1 offset:52608
	v_fma_mixlo_f16 v1, v9, v61, 0
	ds_write_b16 v0, v1 offset:52672
	v_fma_mixlo_f16 v1, v26, v62, 0
	ds_write_b16 v0, v1 offset:53248
	v_fma_mixlo_f16 v1, v10, v62, 0
	ds_write_b16 v0, v1 offset:53312
	v_fma_mixlo_f16 v1, v27, v60, 0
	ds_write_b16 v0, v1 offset:53376
	v_fma_mixlo_f16 v1, v11, v60, 0
	ds_write_b16 v0, v1 offset:53440
	v_fma_mixlo_f16 v1, v28, v59, 0
	ds_write_b16 v0, v1 offset:53504
	v_fma_mixlo_f16 v1, v12, v59, 0
	ds_write_b16 v0, v1 offset:53568
	v_fma_mixlo_f16 v1, v29, v58, 0
	ds_write_b16 v0, v1 offset:53632
	v_fma_mixlo_f16 v1, v13, v58, 0
	ds_write_b16 v0, v1 offset:53696
	v_fma_mixlo_f16 v1, v30, v57, 0
	ds_write_b16 v0, v1 offset:54272
	v_fma_mixlo_f16 v1, v14, v57, 0
	ds_write_b16 v0, v1 offset:54336
	v_fma_mixlo_f16 v1, v31, v56, 0
	ds_write_b16 v0, v1 offset:54400
	v_fma_mixlo_f16 v1, v15, v56, 0
	ds_write_b16 v0, v1 offset:54464
	v_fma_mixlo_f16 v1, v32, v55, 0
	ds_write_b16 v0, v1 offset:54528
	v_fma_mixlo_f16 v1, v16, v55, 0
	ds_write_b16 v0, v1 offset:54592
	v_fma_mixlo_f16 v1, v33, v54, 0
	ds_write_b16 v0, v1 offset:54656
	v_fma_mixlo_f16 v1, v17, v54, 0
	ds_write_b16 v0, v1 offset:54720
	v_and_b32_e32 v0, 56, v183
	v_lshlrev_b32_e32 v8, 1, v0
	v_lshrrev_b32_e32 v14, 3, v182
	v_or_b32_e32 v15, s2, v8
	s_waitcnt lgkmcnt(0)
	v_lshl_or_b32 v0, v14, 7, v15
	v_or_b32_e32 v16, 8, v14
	ds_read_b128 v[0:3], v0 offset:51200
	v_lshl_or_b32 v4, v16, 7, v15
	s_add_u32 s0, s0, s28
	ds_read_b128 v[4:7], v4 offset:51200
	s_addc_u32 s1, s1, 0
	v_mov_b32_e32 v9, 0
	v_lshl_add_u64 v[10:11], s[0:1], 0, v[8:9]
	v_lshlrev_b32_e32 v8, 11, v14
	v_lshl_add_u64 v[12:13], v[10:11], 0, v[8:9]
	v_lshlrev_b32_e32 v8, 11, v16
	s_waitcnt lgkmcnt(1)
	global_store_dwordx4 v[12:13], v[0:3], off
	s_nop 1
	v_lshl_add_u64 v[0:1], v[10:11], 0, v[8:9]
	s_waitcnt lgkmcnt(0)
	global_store_dwordx4 v[0:1], v[4:7], off
	s_nop 1
	v_or_b32_e32 v4, 16, v14
	v_lshl_or_b32 v0, v4, 7, v15
	v_or_b32_e32 v14, 24, v14
	ds_read_b128 v[0:3], v0 offset:51200
	v_lshlrev_b32_e32 v8, 11, v4
	v_lshl_or_b32 v4, v14, 7, v15
	ds_read_b128 v[4:7], v4 offset:51200
	v_lshl_add_u64 v[12:13], v[10:11], 0, v[8:9]
	v_lshlrev_b32_e32 v8, 11, v14
	s_waitcnt lgkmcnt(1)
	global_store_dwordx4 v[12:13], v[0:3], off
	s_nop 1
	v_lshl_add_u64 v[0:1], v[10:11], 0, v[8:9]
	s_waitcnt lgkmcnt(0)
	global_store_dwordx4 v[0:1], v[4:7], off
	s_waitcnt lgkmcnt(0)
	s_barrier
	s_cmp_lg_u32 s47, 0
	s_cbranch_scc1 .Lattn_done
	s_mov_b32 s47, 1
	s_mov_b64 s[0:1], s[44:45]
	s_add_i32 s2, s46, 0x100
	v_mov_b32_e32 v0, v220
	s_mov_b64 exec, -1
	s_branch .Lattn_again
.Lattn_done:
	s_endpgm
.LBB1_59:
	global_load_dwordx4 v[54:57], v[186:187], off
	global_load_dwordx4 v[50:53], v[186:187], off offset:16
	v_lshlrev_b64 v[58:59], v200, 1
	v_or_b32_e32 v60, 8, v200
	v_lshlrev_b64 v[60:61], v60, 1
	v_mov_b32_e32 v98, 0xceabfb8f
	v_or_b32_e32 v62, 2, v200
	v_or_b32_e32 v64, 10, v200
	v_lshlrev_b64 v[62:63], v62, 1
	v_lshlrev_b64 v[64:65], v64, 1
	v_or_b32_e32 v66, 4, v200
	v_or_b32_e32 v68, 12, v200
	v_lshlrev_b64 v[66:67], v66, 1
	v_lshlrev_b64 v[68:69], v68, 1
	s_waitcnt vmcnt(1)
	v_and_b32_e32 v71, v55, v59
	v_and_b32_e32 v70, v54, v58
	v_and_b32_e32 v73, v55, v61
	v_and_b32_e32 v72, v54, v60
	v_cmp_ne_u64_e32 vcc, 0, v[70:71]
	v_and_b32_e32 v75, v57, v59
	v_and_b32_e32 v74, v56, v58
	v_cndmask_b32_e32 v34, v98, v34, vcc
	v_cmp_ne_u64_e32 vcc, 0, v[72:73]
	v_and_b32_e32 v77, v57, v61
	v_and_b32_e32 v76, v56, v60
	v_cndmask_b32_e32 v18, v98, v18, vcc
	v_cmp_ne_u64_e32 vcc, 0, v[74:75]
	s_waitcnt vmcnt(0)
	v_and_b32_e32 v79, v51, v59
	v_and_b32_e32 v78, v50, v58
	v_cndmask_b32_e32 v35, v98, v35, vcc
	v_cmp_ne_u64_e32 vcc, 0, v[76:77]
	v_and_b32_e32 v81, v51, v61
	v_and_b32_e32 v80, v50, v60
	v_cndmask_b32_e32 v19, v98, v19, vcc
	v_cmp_ne_u64_e32 vcc, 0, v[78:79]
	v_and_b32_e32 v59, v53, v59
	v_and_b32_e32 v58, v52, v58
	v_cndmask_b32_e32 v36, v98, v36, vcc
	v_cmp_ne_u64_e32 vcc, 0, v[80:81]
	v_and_b32_e32 v61, v53, v61
	v_and_b32_e32 v60, v52, v60
	v_cndmask_b32_e32 v20, v98, v20, vcc
	v_cmp_ne_u64_e32 vcc, 0, v[58:59]
	v_and_b32_e32 v85, v55, v63
	v_and_b32_e32 v84, v54, v62
	v_cndmask_b32_e32 v37, v98, v37, vcc
	v_cmp_ne_u64_e32 vcc, 0, v[60:61]
	v_and_b32_e32 v87, v55, v65
	v_and_b32_e32 v86, v54, v64
	v_cndmask_b32_e32 v21, v98, v21, vcc
	v_cmp_ne_u64_e32 vcc, 0, v[84:85]
	v_and_b32_e32 v89, v57, v63
	v_and_b32_e32 v88, v56, v62
	v_cndmask_b32_e32 v38, v98, v38, vcc
	v_cmp_ne_u64_e32 vcc, 0, v[86:87]
	v_and_b32_e32 v91, v57, v65
	v_and_b32_e32 v90, v56, v64
	v_cndmask_b32_e32 v22, v98, v22, vcc
	v_cmp_ne_u64_e32 vcc, 0, v[88:89]
	v_and_b32_e32 v93, v51, v63
	v_and_b32_e32 v92, v50, v62
	v_cndmask_b32_e32 v39, v98, v39, vcc
	v_cmp_ne_u64_e32 vcc, 0, v[90:91]
	v_and_b32_e32 v95, v51, v65
	v_and_b32_e32 v94, v50, v64
	v_cndmask_b32_e32 v23, v98, v23, vcc
	v_cmp_ne_u64_e32 vcc, 0, v[92:93]
	v_and_b32_e32 v63, v53, v63
	v_and_b32_e32 v62, v52, v62
	v_cndmask_b32_e32 v40, v98, v40, vcc
	v_cmp_ne_u64_e32 vcc, 0, v[94:95]
	v_and_b32_e32 v65, v53, v65
	v_and_b32_e32 v64, v52, v64
	v_cndmask_b32_e32 v24, v98, v24, vcc
	v_cmp_ne_u64_e32 vcc, 0, v[62:63]
	v_and_b32_e32 v97, v55, v67
	v_and_b32_e32 v96, v54, v66
	v_cndmask_b32_e32 v41, v98, v41, vcc
	v_cmp_ne_u64_e32 vcc, 0, v[64:65]
	v_and_b32_e32 v59, v55, v69
	v_and_b32_e32 v58, v54, v68
	v_cndmask_b32_e32 v25, v98, v25, vcc
	v_cmp_ne_u64_e32 vcc, 0, v[96:97]
	s_nop 1
	v_cndmask_b32_e32 v42, v98, v42, vcc
	v_cmp_ne_u64_e32 vcc, 0, v[58:59]
	v_and_b32_e32 v59, v57, v67
	v_and_b32_e32 v58, v56, v66
	v_cndmask_b32_e32 v26, v98, v26, vcc
	v_cmp_ne_u64_e32 vcc, 0, v[58:59]
	v_and_b32_e32 v59, v57, v69
	v_and_b32_e32 v58, v56, v68
	v_cndmask_b32_e32 v43, v98, v43, vcc
	v_cmp_ne_u64_e32 vcc, 0, v[58:59]
	v_and_b32_e32 v59, v51, v67
	v_and_b32_e32 v58, v50, v66
	v_cndmask_b32_e32 v27, v98, v27, vcc
	v_cmp_ne_u64_e32 vcc, 0, v[58:59]
	v_and_b32_e32 v59, v51, v69
	v_and_b32_e32 v58, v50, v68
	v_cndmask_b32_e32 v44, v98, v44, vcc
	v_cmp_ne_u64_e32 vcc, 0, v[58:59]
	v_and_b32_e32 v59, v53, v67
	v_and_b32_e32 v58, v52, v66
	v_cndmask_b32_e32 v28, v98, v28, vcc
	v_cmp_ne_u64_e32 vcc, 0, v[58:59]
	v_and_b32_e32 v59, v53, v69
	v_and_b32_e32 v58, v52, v68
	v_cndmask_b32_e32 v45, v98, v45, vcc
	v_cmp_ne_u64_e32 vcc, 0, v[58:59]
	v_or_b32_e32 v58, 6, v200
	v_lshlrev_b64 v[58:59], v58, 1
	v_and_b32_e32 v61, v55, v59
	v_and_b32_e32 v60, v54, v58
	v_cndmask_b32_e32 v29, v98, v29, vcc
	v_cmp_ne_u64_e32 vcc, 0, v[60:61]
	v_or_b32_e32 v60, 14, v200
	v_lshlrev_b64 v[60:61], v60, 1
	v_and_b32_e32 v55, v55, v61
	v_and_b32_e32 v54, v54, v60
	v_cndmask_b32_e32 v46, v98, v46, vcc
	v_cmp_ne_u64_e32 vcc, 0, v[54:55]
	v_and_b32_e32 v55, v57, v59
	v_and_b32_e32 v54, v56, v58
	v_cndmask_b32_e32 v30, v98, v30, vcc
	v_cmp_ne_u64_e32 vcc, 0, v[54:55]
	v_and_b32_e32 v55, v57, v61
	v_and_b32_e32 v54, v56, v60
	v_cndmask_b32_e32 v47, v98, v47, vcc
	v_cmp_ne_u64_e32 vcc, 0, v[54:55]
	v_and_b32_e32 v55, v51, v59
	v_and_b32_e32 v54, v50, v58
	v_cndmask_b32_e32 v31, v98, v31, vcc
	v_cmp_ne_u64_e32 vcc, 0, v[54:55]
	v_and_b32_e32 v51, v51, v61
	v_and_b32_e32 v50, v50, v60
	v_cndmask_b32_e32 v48, v98, v48, vcc
	v_cmp_ne_u64_e32 vcc, 0, v[50:51]
	v_and_b32_e32 v51, v53, v59
	v_and_b32_e32 v50, v52, v58
	v_cndmask_b32_e32 v32, v98, v32, vcc
	v_cmp_ne_u64_e32 vcc, 0, v[50:51]
	v_and_b32_e32 v51, v53, v61
	v_and_b32_e32 v50, v52, v60
	v_cndmask_b32_e32 v49, v98, v49, vcc
	v_cmp_ne_u64_e32 vcc, 0, v[50:51]
	s_nop 1
	v_cndmask_b32_e32 v33, v98, v33, vcc
	s_branch .LBB1_1

.LBB1_65:
	global_load_ushort v51, v[52:53], off offset:-64
	global_load_ushort v71, v[52:53], off
	v_add_u32_e32 v70, 2, v70
	v_cmp_lt_u32_e32 vcc, s6, v70
	v_lshl_add_u64 v[52:53], v[52:53], 0, s[2:3]
	s_or_b64 s[0:1], vcc, s[0:1]
	s_waitcnt vmcnt(1)
	v_cvt_f32_f16_e32 v51, v51
	s_waitcnt vmcnt(0)
	v_cvt_f32_f16_e32 v71, v71
	v_add_f32_e32 v0, v0, v51
	v_add_f32_e32 v1, v1, v71
	s_andn2_b64 exec, exec, s[0:1]
	s_cbranch_execnz .LBB1_65
	s_or_b64 exec, exec, s[0:1]
	v_mov_b32_e32 v51, v0
	s_nop 1
	v_permlane32_swap_b32_e32 v0, v51
	v_add_f32_e32 v0, v0, v51
	v_mov_b32_e32 v51, v1
	s_nop 1
	v_permlane32_swap_b32_e32 v1, v51
	v_add_f32_e32 v1, v1, v51
	v_mul_f32_e32 v0, 0x3a000000, v0
	v_mul_f32_e32 v1, 0x3a000000, v1
	v_cmp_eq_f32_e32 vcc, 0, v46
	s_nop 1
	v_cndmask_b32_e32 v2, v2, v1, vcc
	v_cndmask_b32_e32 v18, v18, v0, vcc
	v_cndmask_b32_e64 v69, v69, 1.0, vcc
	v_cmp_eq_f32_e32 vcc, 0, v47
	s_nop 1
	v_cndmask_b32_e32 v3, v3, v1, vcc
	v_cndmask_b32_e32 v19, v19, v0, vcc
	v_cndmask_b32_e64 v68, v68, 1.0, vcc
	v_cmp_eq_f32_e32 vcc, 0, v48
	s_nop 1
	v_cndmask_b32_e32 v4, v4, v1, vcc
	v_cndmask_b32_e32 v20, v20, v0, vcc
	v_cndmask_b32_e64 v67, v67, 1.0, vcc
	v_cmp_eq_f32_e32 vcc, 0, v49
	s_nop 1
	v_cndmask_b32_e32 v5, v5, v1, vcc
	v_cndmask_b32_e32 v21, v21, v0, vcc
	v_cndmask_b32_e64 v66, v66, 1.0, vcc
	v_cmp_eq_f32_e32 vcc, 0, v42
	s_nop 1
	v_cndmask_b32_e32 v6, v6, v1, vcc
	v_cndmask_b32_e32 v22, v22, v0, vcc
	v_cndmask_b32_e64 v64, v64, 1.0, vcc
	v_cmp_eq_f32_e32 vcc, 0, v43
	s_nop 1
	v_cndmask_b32_e32 v7, v7, v1, vcc
	v_cndmask_b32_e32 v23, v23, v0, vcc
	v_cndmask_b32_e64 v65, v65, 1.0, vcc
	v_cmp_eq_f32_e32 vcc, 0, v44
	s_nop 1
	v_cndmask_b32_e32 v8, v8, v1, vcc
	v_cndmask_b32_e32 v24, v24, v0, vcc
	v_cndmask_b32_e64 v63, v63, 1.0, vcc
	v_cmp_eq_f32_e32 vcc, 0, v45
	s_nop 1
	v_cndmask_b32_e32 v9, v9, v1, vcc
	v_cndmask_b32_e32 v25, v25, v0, vcc
	v_cndmask_b32_e64 v61, v61, 1.0, vcc
	v_cmp_eq_f32_e32 vcc, 0, v38
	s_nop 1
	v_cndmask_b32_e32 v10, v10, v1, vcc
	v_cndmask_b32_e32 v26, v26, v0, vcc
	v_cndmask_b32_e64 v62, v62, 1.0, vcc
	v_cmp_eq_f32_e32 vcc, 0, v39
	s_nop 1
	v_cndmask_b32_e32 v11, v11, v1, vcc
	v_cndmask_b32_e32 v27, v27, v0, vcc
	v_cndmask_b32_e64 v60, v60, 1.0, vcc
	v_cmp_eq_f32_e32 vcc, 0, v40
	s_nop 1
	v_cndmask_b32_e32 v12, v12, v1, vcc
	v_cndmask_b32_e32 v28, v28, v0, vcc
	v_cndmask_b32_e64 v59, v59, 1.0, vcc
	v_cmp_eq_f32_e32 vcc, 0, v41
	s_nop 1
	v_cndmask_b32_e32 v13, v13, v1, vcc
	v_cndmask_b32_e32 v29, v29, v0, vcc
	v_cndmask_b32_e64 v58, v58, 1.0, vcc
	v_cmp_eq_f32_e32 vcc, 0, v34
	s_nop 1
	v_cndmask_b32_e32 v14, v14, v1, vcc
	v_cndmask_b32_e32 v30, v30, v0, vcc
	v_cndmask_b32_e64 v57, v57, 1.0, vcc
	v_cmp_eq_f32_e32 vcc, 0, v35
	s_nop 1
	v_cndmask_b32_e32 v15, v15, v1, vcc
	v_cndmask_b32_e32 v31, v31, v0, vcc
	v_cndmask_b32_e64 v56, v56, 1.0, vcc
	v_cmp_eq_f32_e32 vcc, 0, v36
	s_nop 1
	v_cndmask_b32_e32 v16, v16, v1, vcc
	v_cndmask_b32_e32 v32, v32, v0, vcc
	v_cndmask_b32_e64 v55, v55, 1.0, vcc
	v_cmp_eq_f32_e32 vcc, 0, v37
	s_nop 1
	v_cndmask_b32_e32 v17, v17, v1, vcc
	v_cndmask_b32_e32 v33, v33, v0, vcc
	v_cndmask_b32_e64 v54, v54, 1.0, vcc
	s_branch .LBB1_58
	s_nop 0
	s_nop 0
	s_nop 0
	s_nop 0
	s_nop 0
	s_nop 0
	s_nop 0
	s_nop 0
	s_nop 0
	s_nop 0
	s_nop 0
	s_nop 0
	s_nop 0
	s_nop 0
	s_nop 0
	s_nop 0
	s_nop 0
	s_nop 0
	s_nop 0
	s_nop 0
	s_nop 0
	s_nop 0
	s_nop 0
	s_nop 0
	s_nop 0
	s_nop 0
	s_nop 0
	s_nop 0
	s_nop 0
	s_nop 0
	s_nop 0
	s_nop 0
	s_nop 0
	s_nop 0
	s_nop 0
	s_nop 0
	s_nop 0
	s_nop 0
	s_nop 0
	s_nop 0
	s_nop 0
	s_nop 0
	s_nop 0
	s_nop 0
	s_nop 0
	s_nop 0
	s_nop 0
	s_endpgm

	.amdhsa_kernel _ZN4attn11attn_kernelEPKDF16_S1_S1_PDF16_PKyPKh
		.amdhsa_group_segment_fixed_size 83968
		.amdhsa_private_segment_fixed_size 0
		.amdhsa_kernarg_size 48
		.amdhsa_user_sgpr_count 2
		.amdhsa_user_sgpr_dispatch_ptr 0
		.amdhsa_user_sgpr_queue_ptr 0
		.amdhsa_user_sgpr_kernarg_segment_ptr 1
		.amdhsa_user_sgpr_dispatch_id 0
		.amdhsa_user_sgpr_kernarg_preload_length 0
		.amdhsa_user_sgpr_kernarg_preload_offset 0
		.amdhsa_user_sgpr_private_segment_size 0
		.amdhsa_uses_dynamic_stack 0
		.amdhsa_enable_private_segment 0
		.amdhsa_system_sgpr_workgroup_id_x 1
		.amdhsa_system_sgpr_workgroup_id_y 0
		.amdhsa_system_sgpr_workgroup_id_z 0
		.amdhsa_system_sgpr_workgroup_info 0
		.amdhsa_system_vgpr_workitem_id 0
		.amdhsa_next_free_vgpr 221
		.amdhsa_next_free_sgpr 96
		.amdhsa_accum_offset 224
		.amdhsa_reserve_vcc 1
		.amdhsa_float_round_mode_32 0
		.amdhsa_float_round_mode_16_64 0
		.amdhsa_float_denorm_mode_32 3
		.amdhsa_float_denorm_mode_16_64 3
		.amdhsa_dx10_clamp 1
		.amdhsa_ieee_mode 1
		.amdhsa_fp16_overflow 0
		.amdhsa_tg_split 0
		.amdhsa_exception_fp_ieee_invalid_op 0
		.amdhsa_exception_fp_denorm_src 0
		.amdhsa_exception_fp_ieee_div_zero 0
		.amdhsa_exception_fp_ieee_overflow 0
		.amdhsa_exception_fp_ieee_underflow 0
		.amdhsa_exception_fp_ieee_inexact 0
		.amdhsa_exception_int_div_zero 0
	.end_amdhsa_kernel

amdhsa.kernels:
  - .agpr_count:     0
    .args:
      - .offset:         0
        .size:           64
        .value_kind:     by_value
    .group_segment_fixed_size: 0
    .kernarg_segment_align: 8
    .kernarg_segment_size: 64
    .language:       OpenCL C
    .language_version:
      - 2
      - 0
    .max_flat_workgroup_size: 256
    .name:           _Z11prep_kernel8PrepArgs
    .private_segment_fixed_size: 0
    .sgpr_count:     22
    .sgpr_spill_count: 0
    .symbol:         _Z11prep_kernel8PrepArgs.kd
    .uniform_work_group_size: 1
    .uses_dynamic_stack: false
    .vgpr_count:     38
    .vgpr_spill_count: 0
    .wavefront_size: 64
  - .agpr_count:     0
    .args:
      - .address_space:  global
        .offset:         0
        .size:           8
        .value_kind:     global_buffer
      - .address_space:  global
        .offset:         8
        .size:           8
        .value_kind:     global_buffer
      - .address_space:  global
        .offset:         16
        .size:           8
        .value_kind:     global_buffer
      - .address_space:  global
        .offset:         24
        .size:           8
        .value_kind:     global_buffer
      - .address_space:  global
        .offset:         32
        .size:           8
        .value_kind:     global_buffer
      - .address_space:  global
        .offset:         40
        .size:           8
        .value_kind:     global_buffer
    .group_segment_fixed_size: 83968
    .kernarg_segment_align: 8
    .kernarg_segment_size: 48
    .language:       OpenCL C
    .language_version:
      - 2
      - 0
    .max_flat_workgroup_size: 512
    .name:           _ZN4attn11attn_kernelEPKDF16_S1_S1_PDF16_PKyPKh
    .private_segment_fixed_size: 0
    .sgpr_count:     48
    .sgpr_spill_count: 0
    .symbol:         _ZN4attn11attn_kernelEPKDF16_S1_S1_PDF16_PKyPKh.kd
    .uniform_work_group_size: 1
    .uses_dynamic_stack: false
    .vgpr_count:     221
    .vgpr_spill_count: 0
    .wavefront_size: 64
  - .agpr_count:     0
    .args:
      - .offset:         0
        .size:           120
        .value_kind:     by_value
      - .offset:         120
        .size:           4
        .value_kind:     hidden_block_count_x
      - .offset:         124
        .size:           4
        .value_kind:     hidden_block_count_y
      - .offset:         128
        .size:           4
        .value_kind:     hidden_block_count_z
      - .offset:         132
        .size:           2
        .value_kind:     hidden_group_size_x
      - .offset:         134
        .size:           2
        .value_kind:     hidden_group_size_y
      - .offset:         136
        .size:           2
        .value_kind:     hidden_group_size_z
      - .offset:         138
        .size:           2
        .value_kind:     hidden_remainder_x
      - .offset:         140
        .size:           2
        .value_kind:     hidden_remainder_y
      - .offset:         142
        .size:           2
        .value_kind:     hidden_remainder_z
      - .offset:         160
        .size:           8
        .value_kind:     hidden_global_offset_x
      - .offset:         168
        .size:           8
        .value_kind:     hidden_global_offset_y
      - .offset:         176
        .size:           8
        .value_kind:     hidden_global_offset_z
      - .offset:         184
        .size:           2
        .value_kind:     hidden_grid_dims
    .group_segment_fixed_size: 131072
    .kernarg_segment_align: 8
    .kernarg_segment_size: 376
    .language:       OpenCL C
    .language_version:
      - 2
      - 0
    .max_flat_workgroup_size: 512
    .name:           _ZN4gemm15gemm128r_kernelILb1ELi0ELi3ELb1EEEvNS_7Args128E
    .private_segment_fixed_size: 0
    .sgpr_count:     104
    .sgpr_spill_count: 0
    .symbol:         _ZN4gemm15gemm128r_kernelILb1ELi0ELi3ELb1EEEvNS_7Args128E.kd
    .uniform_work_group_size: 1
    .uses_dynamic_stack: false
    .vgpr_count:     211
    .vgpr_spill_count: 0
    .wavefront_size: 64
  - .agpr_count:     0
    .args:
      - .offset:         0
        .size:           120
        .value_kind:     by_value
      - .offset:         120
        .size:           4
        .value_kind:     hidden_block_count_x
      - .offset:         124
        .size:           4
        .value_kind:     hidden_block_count_y
      - .offset:         128
        .size:           4
        .value_kind:     hidden_block_count_z
      - .offset:         132
        .size:           2
        .value_kind:     hidden_group_size_x
      - .offset:         134
        .size:           2
        .value_kind:     hidden_group_size_y
      - .offset:         136
        .size:           2
        .value_kind:     hidden_group_size_z
      - .offset:         138
        .size:           2
        .value_kind:     hidden_remainder_x
      - .offset:         140
        .size:           2
        .value_kind:     hidden_remainder_y
      - .offset:         142
        .size:           2
        .value_kind:     hidden_remainder_z
      - .offset:         160
        .size:           8
        .value_kind:     hidden_global_offset_x
      - .offset:         168
        .size:           8
        .value_kind:     hidden_global_offset_y
      - .offset:         176
        .size:           8
        .value_kind:     hidden_global_offset_z
      - .offset:         184
        .size:           2
        .value_kind:     hidden_grid_dims
    .group_segment_fixed_size: 131072
    .kernarg_segment_align: 8
    .kernarg_segment_size: 376
    .language:       OpenCL C
    .language_version:
      - 2
      - 0
    .max_flat_workgroup_size: 512
    .name:           _ZN4gemm15gemm128r_kernelILb0ELi1ELi1ELb0EEEvNS_7Args128E
    .private_segment_fixed_size: 0
    .sgpr_count:     75
    .sgpr_spill_count: 0
    .symbol:         _ZN4gemm15gemm128r_kernelILb0ELi1ELi1ELb0EEEvNS_7Args128E.kd
    .uniform_work_group_size: 1
    .uses_dynamic_stack: false
    .vgpr_count:     178
    .vgpr_spill_count: 0
    .wavefront_size: 64
